# adds skip-zero-accumulator rescale + v_permlane32_swap row max to (P4a epilogue hoist + vm_wait direct branches + no-copy)
# baseline (speedup 1.0000x reference)
.LBB0_730:
	s_nop 6
	v_max_f32_e32 v66, v131, v131
	v_max_f32_e32 v67, v130, v130
	v_max_f32_e32 v66, v67, v66
	v_max3_f32 v66, v66, v132, v133
	v_max3_f32 v66, v66, v134, v135
	v_max3_f32 v66, v66, v136, v137
	v_max3_f32 v66, v66, v138, v139
	v_max3_f32 v66, v66, v140, v141
	v_max3_f32 v66, v66, v142, v143
	v_max3_f32 v66, v66, v144, v145
	v_mov_b32_e32 v67, v66
	s_nop 1
	v_permlane32_swap_b32_e32 v67, v66
	v_max_f32_e32 v66, v66, v67
	v_add_f32_e32 v67, 0x40c00000, v231
	v_cmp_gt_f32_e32 vcc, v66, v67
	s_nop 1
	v_cndmask_b32_e32 v233, v231, v66, vcc
	v_sub_f32_e32 v66, v231, v233
	v_exp_f32_e32 v146, v66
	s_cbranch_vccz .LBB0_732
	v_cmp_ne_u32_e32 vcc, 0xf149f2ca, v231
	s_cbranch_vccz .LBB0_732
	v_pk_mul_f32 v[64:65], v[64:65], v[146:147] op_sel_hi:[1,0]
	v_pk_mul_f32 v[62:63], v[62:63], v[146:147] op_sel_hi:[1,0]
	v_pk_mul_f32 v[60:61], v[60:61], v[146:147] op_sel_hi:[1,0]
	v_pk_mul_f32 v[58:59], v[58:59], v[146:147] op_sel_hi:[1,0]
	v_pk_mul_f32 v[56:57], v[56:57], v[146:147] op_sel_hi:[1,0]
	v_pk_mul_f32 v[54:55], v[54:55], v[146:147] op_sel_hi:[1,0]
	v_pk_mul_f32 v[52:53], v[52:53], v[146:147] op_sel_hi:[1,0]
	v_pk_mul_f32 v[50:51], v[50:51], v[146:147] op_sel_hi:[1,0]
	v_pk_mul_f32 v[48:49], v[48:49], v[146:147] op_sel_hi:[1,0]
	v_pk_mul_f32 v[46:47], v[46:47], v[146:147] op_sel_hi:[1,0]
	v_pk_mul_f32 v[44:45], v[44:45], v[146:147] op_sel_hi:[1,0]
	v_pk_mul_f32 v[42:43], v[42:43], v[146:147] op_sel_hi:[1,0]
	v_pk_mul_f32 v[40:41], v[40:41], v[146:147] op_sel_hi:[1,0]
	v_pk_mul_f32 v[38:39], v[38:39], v[146:147] op_sel_hi:[1,0]
	v_pk_mul_f32 v[36:37], v[36:37], v[146:147] op_sel_hi:[1,0]
	v_pk_mul_f32 v[34:35], v[34:35], v[146:147] op_sel_hi:[1,0]
	v_pk_mul_f32 v[32:33], v[32:33], v[146:147] op_sel_hi:[1,0]
	v_pk_mul_f32 v[30:31], v[30:31], v[146:147] op_sel_hi:[1,0]
	v_pk_mul_f32 v[28:29], v[28:29], v[146:147] op_sel_hi:[1,0]
	v_pk_mul_f32 v[26:27], v[26:27], v[146:147] op_sel_hi:[1,0]
	v_pk_mul_f32 v[24:25], v[24:25], v[146:147] op_sel_hi:[1,0]
	v_pk_mul_f32 v[22:23], v[22:23], v[146:147] op_sel_hi:[1,0]
	v_pk_mul_f32 v[20:21], v[20:21], v[146:147] op_sel_hi:[1,0]
	v_pk_mul_f32 v[18:19], v[18:19], v[146:147] op_sel_hi:[1,0]
	v_pk_mul_f32 v[16:17], v[16:17], v[146:147] op_sel_hi:[1,0]
	v_pk_mul_f32 v[14:15], v[14:15], v[146:147] op_sel_hi:[1,0]
	v_pk_mul_f32 v[12:13], v[12:13], v[146:147] op_sel_hi:[1,0]
	v_pk_mul_f32 v[10:11], v[10:11], v[146:147] op_sel_hi:[1,0]
	v_pk_mul_f32 v[8:9], v[8:9], v[146:147] op_sel_hi:[1,0]
	v_pk_mul_f32 v[6:7], v[6:7], v[146:147] op_sel_hi:[1,0]
	v_pk_mul_f32 v[4:5], v[4:5], v[146:147] op_sel_hi:[1,0]
	v_pk_mul_f32 v[2:3], v[2:3], v[146:147] op_sel_hi:[1,0]
	s_branch .LBB0_733

.LBB0_800:
	s_nop 6
	v_max_f32_e32 v66, v131, v131
	v_max_f32_e32 v67, v130, v130
	v_max_f32_e32 v66, v67, v66
	v_max3_f32 v66, v66, v132, v133
	v_max3_f32 v66, v66, v134, v135
	v_max3_f32 v66, v66, v136, v137
	v_max3_f32 v66, v66, v138, v139
	v_max3_f32 v66, v66, v140, v141
	v_max3_f32 v66, v66, v142, v143
	v_max3_f32 v66, v66, v144, v145
	v_mov_b32_e32 v67, v66
	s_nop 1
	v_permlane32_swap_b32_e32 v67, v66
	v_max_f32_e32 v66, v66, v67
	v_add_f32_e32 v67, 0x40c00000, v233
	v_cmp_gt_f32_e32 vcc, v66, v67
	s_nop 1
	v_cndmask_b32_e32 v235, v233, v66, vcc
	v_sub_f32_e32 v66, v233, v235
	v_exp_f32_e32 v146, v66
	s_cbranch_vccz .LBB0_802
	v_cmp_ne_u32_e32 vcc, 0xf149f2ca, v233
	s_cbranch_vccz .LBB0_802
	v_pk_mul_f32 v[64:65], v[64:65], v[146:147] op_sel_hi:[1,0]
	v_pk_mul_f32 v[62:63], v[62:63], v[146:147] op_sel_hi:[1,0]
	v_pk_mul_f32 v[60:61], v[60:61], v[146:147] op_sel_hi:[1,0]
	v_pk_mul_f32 v[58:59], v[58:59], v[146:147] op_sel_hi:[1,0]
	v_pk_mul_f32 v[56:57], v[56:57], v[146:147] op_sel_hi:[1,0]
	v_pk_mul_f32 v[54:55], v[54:55], v[146:147] op_sel_hi:[1,0]
	v_pk_mul_f32 v[52:53], v[52:53], v[146:147] op_sel_hi:[1,0]
	v_pk_mul_f32 v[50:51], v[50:51], v[146:147] op_sel_hi:[1,0]
	v_pk_mul_f32 v[48:49], v[48:49], v[146:147] op_sel_hi:[1,0]
	v_pk_mul_f32 v[46:47], v[46:47], v[146:147] op_sel_hi:[1,0]
	v_pk_mul_f32 v[44:45], v[44:45], v[146:147] op_sel_hi:[1,0]
	v_pk_mul_f32 v[42:43], v[42:43], v[146:147] op_sel_hi:[1,0]
	v_pk_mul_f32 v[40:41], v[40:41], v[146:147] op_sel_hi:[1,0]
	v_pk_mul_f32 v[38:39], v[38:39], v[146:147] op_sel_hi:[1,0]
	v_pk_mul_f32 v[36:37], v[36:37], v[146:147] op_sel_hi:[1,0]
	v_pk_mul_f32 v[34:35], v[34:35], v[146:147] op_sel_hi:[1,0]
	v_pk_mul_f32 v[32:33], v[32:33], v[146:147] op_sel_hi:[1,0]
	v_pk_mul_f32 v[30:31], v[30:31], v[146:147] op_sel_hi:[1,0]
	v_pk_mul_f32 v[28:29], v[28:29], v[146:147] op_sel_hi:[1,0]
	v_pk_mul_f32 v[26:27], v[26:27], v[146:147] op_sel_hi:[1,0]
	v_pk_mul_f32 v[24:25], v[24:25], v[146:147] op_sel_hi:[1,0]
	v_pk_mul_f32 v[22:23], v[22:23], v[146:147] op_sel_hi:[1,0]
	v_pk_mul_f32 v[20:21], v[20:21], v[146:147] op_sel_hi:[1,0]
	v_pk_mul_f32 v[18:19], v[18:19], v[146:147] op_sel_hi:[1,0]
	v_pk_mul_f32 v[16:17], v[16:17], v[146:147] op_sel_hi:[1,0]
	v_pk_mul_f32 v[14:15], v[14:15], v[146:147] op_sel_hi:[1,0]
	v_pk_mul_f32 v[12:13], v[12:13], v[146:147] op_sel_hi:[1,0]
	v_pk_mul_f32 v[10:11], v[10:11], v[146:147] op_sel_hi:[1,0]
	v_pk_mul_f32 v[8:9], v[8:9], v[146:147] op_sel_hi:[1,0]
	v_pk_mul_f32 v[6:7], v[6:7], v[146:147] op_sel_hi:[1,0]
	v_pk_mul_f32 v[4:5], v[4:5], v[146:147] op_sel_hi:[1,0]
	v_pk_mul_f32 v[2:3], v[2:3], v[146:147] op_sel_hi:[1,0]
	s_branch .LBB0_803
